# conversion share moved into the layer-0 MoE idle tail raised from 6 to 8 items per wave (P9 keeps 512 items instead of 1920); on top of v62
# speedup vs baseline: 1.0006x; 1.0006x over previous
.LBB0_1151:
	v_mov_b32_e32 v1, 0x224f0
	ds_read_b32 v1, v1
	s_waitcnt lgkmcnt(0)
	v_readfirstlane_b32 s0, v1
	s_lshl_b32 s0, s0, 2
	s_sub_i32 s0, s0, s33
	s_max_i32 s0, s0, 0
	s_mul_i32 s0, s0, 3
	s_sub_i32 s1, s33, s0
	s_cmp_lt_i32 s1, 1
	s_cbranch_scc1 .Lcv_skip
	s_cmp_lt_i32 s95, s0
	s_cbranch_scc1 .Lcv_skip
	s_lshl_b32 s12, s1, 3
	s_mul_i32 s13, s1, 64
	s_min_i32 s13, s13, 0x1800
	s_sub_i32 s14, s95, s0
	s_lshl_b32 s14, s14, 3
	s_add_i32 s34, s14, s92
	s_addk_i32 s12, 0x200
	s_cmp_ge_i32 s34, s13
	s_cbranch_scc1 .Lcv_skip
	s_mov_b64 s[4:5], -1
	s_cmp_lt_i32 s34, s13
	s_cselect_b64 s[6:7], -1, 0
	s_and_b64 s[8:9], s[6:7], exec
	s_cselect_b32 s16, s34, 0
	s_cmpk_gt_i32 s16, 0xfff
	s_cbranch_scc0 .Lcv1379
	s_bfe_u32 s8, s16, 0x20007
	s_cmp_lt_i32 s8, 1
	s_mov_b32 s17, 4
	s_cbranch_scc1 .Lcv1384
	s_cmp_eq_u32 s8, 1
	s_cbranch_scc1 .Lcv1381
	s_cmp_eq_u32 s8, 2
	s_cselect_b32 s17, 5, 7
	s_mov_b64 s[4:5], 0
	s_branch .Lcv1382

.LBB0_1374:
	s_cmp_lt_i32 s89, 32
	s_cselect_b64 s[6:7], -1, 0
	s_xor_b64 s[8:9], s[16:17], -1
	s_or_b64 s[6:7], s[6:7], s[8:9]
	s_mov_b64 s[4:5], -1
	s_and_b64 vcc, exec, s[6:7]
	s_cbranch_vccnz .LBB0_1443
	s_lshl_b32 s6, s89, 3
	s_add_i32 s6, s6, s92
	s_add_i32 s34, s6, 0xffffff00
	v_mov_b32_e32 v1, 0x224f0
	ds_read_b32 v1, v1
	s_waitcnt lgkmcnt(0)
	v_readfirstlane_b32 s7, v1
	s_lshl_b32 s7, s7, 2
	s_sub_i32 s7, s7, s33
	s_max_i32 s7, s7, 0
	s_mul_i32 s7, s7, 3
	s_sub_i32 s7, s33, s7
	s_max_i32 s7, s7, 0
	s_mul_i32 s7, s7, 64
	s_min_i32 s7, s7, 0x1800
	s_add_i32 s34, s34, s7
	s_cmpk_lt_i32 s34, 0x1800
	s_cselect_b64 s[6:7], -1, 0
	s_and_b64 s[8:9], s[6:7], exec
	s_cselect_b32 s16, s34, 0
	s_cmpk_gt_i32 s16, 0xfff
	s_cbranch_scc0 .LBB0_1379
	s_bfe_u32 s8, s16, 0x20007
	s_cmp_lt_i32 s8, 1
	s_mov_b32 s17, 4
	s_cbranch_scc1 .LBB0_1384
	s_cmp_eq_u32 s8, 1
	s_cbranch_scc1 .LBB0_1381
	s_cmp_eq_u32 s8, 2
	s_cselect_b32 s17, 5, 7
	s_mov_b64 s[4:5], 0
	s_branch .LBB0_1382
